# baseline (speedup 1.0000x reference)
.LBB1_9:
	s_or_b64 exec, exec, s[6:7]
	v_lshlrev_b32_e32 v3, 12, v0
	v_and_b32_e32 v6, 0x3f8000, v3
	v_mov_b32_e32 v7, 0
	v_lshrrev_b32_e32 v1, 3, v0
	v_lshl_add_u64 v[4:5], s[4:5], 0, v[6:7]
	v_and_b32_e32 v2, 7, v0
	v_mov_b32_e32 v3, v7
	v_lshlrev_b32_e32 v8, 2, v1
	v_add_u32_e32 v8, 0x1000, v8
	v_add_u32_e32 v9, 0x200, v8
	ds_read2_b32 v[16:17], v8 offset1:196
	ds_read2_b32 v[18:19], v9 offset1:196
	v_mov_b32_e32 v14, 1
	v_mov_b32_e32 v15, 2
	s_movk_i32 s3, 0x44
	s_mov_b64 s[14:15], 0x400000
	s_mov_b64 s[22:23], 0x80
	v_cmp_gt_u32_e64 s[24:25], s3, v1
	s_waitcnt lgkmcnt(0)
	v_add_u32_e32 v20, v16, v2
	v_add_u32_e32 v21, v18, v2
	v_cndmask_b32_e64 v19, v18, v19, s[24:25]
	v_lshlrev_b32_e32 v22, 4, v20
	v_mov_b32_e32 v23, 0
	v_lshlrev_b32_e32 v24, 4, v21
	v_mov_b32_e32 v25, 0
	v_lshl_add_u64 v[22:23], v[4:5], 0, v[22:23]
	v_lshl_add_u64 v[24:25], v[4:5], 0, v[24:25]
	v_lshl_add_u64 v[24:25], v[24:25], 0, s[14:15]
	v_add_u32_e32 v26, 8, v20
	v_add_u32_e32 v27, 8, v21
	v_cmp_lt_i32_e64 s[4:5], v20, v17
	v_cmp_lt_i32_e64 s[6:7], v26, v17
	v_cmp_lt_i32_e64 s[12:13], v21, v19
	v_cmp_lt_i32_e64 s[16:17], v27, v19
	v_add_u32_e32 v26, 8, v26
	v_add_u32_e32 v27, 8, v27
	v_cmp_lt_i32_e64 s[18:19], v26, v17
	v_cmp_lt_i32_e64 s[20:21], v27, v19
	s_mov_b64 exec, s[4:5]
	s_cbranch_execz .Lkb_p1_ld0
	global_load_dwordx4 v[36:39], v[22:23], off

.Lkb_p1_ld3:
	s_waitcnt vmcnt(0)
	v_lshlrev_b32_sdwa v31, v15, v48 dst_sel:DWORD dst_unused:UNUSED_PAD src0_sel:DWORD src1_sel:WORD_1
	ds_add_u32 v31, v14 offset:6176
	s_mov_b64 exec, s[12:13]
	v_lshlrev_b32_sdwa v30, v15, v44 dst_sel:DWORD dst_unused:UNUSED_PAD src0_sel:DWORD src1_sel:WORD_1
	ds_add_u32 v30, v14 offset:6176
	s_mov_b64 exec, s[6:7]
	v_lshlrev_b32_sdwa v29, v15, v40 dst_sel:DWORD dst_unused:UNUSED_PAD src0_sel:DWORD src1_sel:WORD_1
	ds_add_u32 v29, v14 offset:6176
	s_mov_b64 exec, s[4:5]
	v_lshlrev_b32_sdwa v28, v15, v36 dst_sel:DWORD dst_unused:UNUSED_PAD src0_sel:DWORD src1_sel:WORD_1
	ds_add_u32 v28, v14 offset:6176
	s_mov_b64 exec, s[18:19]
	s_cbranch_execz .Lkb_p1_a_end
	v_lshl_add_u64 v[32:33], v[22:23], 0, s[22:23]
	v_lshl_add_u64 v[32:33], v[32:33], 0, s[22:23]
	s_mov_b64 s[4:5], 0

.LBB1_21:
	s_or_b64 exec, exec, s[4:5]
	v_lshlrev_b32_e32 v8, 2, v1
	v_add_u32_e32 v8, 0x1000, v8
	v_add_u32_e32 v9, 0x200, v8
	ds_read2_b32 v[16:17], v8 offset1:196
	ds_read2_b32 v[18:19], v9 offset1:196
	v_mov_b32_e32 v11, 1
	v_mov_b32_e32 v12, 2
	s_movk_i32 s3, 0x44
	s_mov_b64 s[14:15], 0x400000
	s_mov_b64 s[22:23], 0x80
	v_cmp_gt_u32_e64 s[24:25], s3, v1
	s_waitcnt lgkmcnt(0)
	v_add_u32_e32 v20, v16, v2
	v_add_u32_e32 v21, v18, v2
	v_cndmask_b32_e64 v19, v18, v19, s[24:25]
	v_lshlrev_b32_e32 v22, 4, v20
	v_mov_b32_e32 v23, 0
	v_lshlrev_b32_e32 v24, 4, v21
	v_mov_b32_e32 v25, 0
	v_lshl_add_u64 v[22:23], v[4:5], 0, v[22:23]
	v_lshl_add_u64 v[24:25], v[4:5], 0, v[24:25]
	v_lshl_add_u64 v[24:25], v[24:25], 0, s[14:15]
	v_add_u32_e32 v26, 8, v20
	v_add_u32_e32 v27, 8, v21
	v_cmp_lt_i32_e64 s[4:5], v20, v17
	v_cmp_lt_i32_e64 s[6:7], v26, v17
	v_cmp_lt_i32_e64 s[12:13], v21, v19
	v_cmp_lt_i32_e64 s[16:17], v27, v19
	v_add_u32_e32 v26, 8, v26
	v_add_u32_e32 v27, 8, v27
	v_cmp_lt_i32_e64 s[18:19], v26, v17
	v_cmp_lt_i32_e64 s[20:21], v27, v19
	s_mov_b64 exec, s[16:17]
	v_lshlrev_b32_sdwa v31, v12, v48 dst_sel:DWORD dst_unused:UNUSED_PAD src0_sel:DWORD src1_sel:WORD_1
	ds_add_rtn_u32 v58, v31, v11 offset:5664
	ds_read_b32 v31, v31 offset:6688
	v_and_b32_e32 v48, 0xffff, v48
	s_mov_b64 exec, s[12:13]
	v_lshlrev_b32_sdwa v30, v12, v44 dst_sel:DWORD dst_unused:UNUSED_PAD src0_sel:DWORD src1_sel:WORD_1
	ds_add_rtn_u32 v56, v30, v11 offset:5664
	ds_read_b32 v30, v30 offset:6688
	v_and_b32_e32 v44, 0xffff, v44
	s_mov_b64 exec, s[6:7]
	v_lshlrev_b32_sdwa v29, v12, v40 dst_sel:DWORD dst_unused:UNUSED_PAD src0_sel:DWORD src1_sel:WORD_1
	ds_add_rtn_u32 v54, v29, v11 offset:5664
	ds_read_b32 v29, v29 offset:6688
	v_and_b32_e32 v40, 0xffff, v40
	s_mov_b64 exec, s[4:5]
	v_lshlrev_b32_sdwa v28, v12, v36 dst_sel:DWORD dst_unused:UNUSED_PAD src0_sel:DWORD src1_sel:WORD_1
	ds_add_rtn_u32 v52, v28, v11 offset:5664
	ds_read_b32 v28, v28 offset:6688
	v_and_b32_e32 v36, 0xffff, v36
	s_waitcnt lgkmcnt(0)
	v_add3_u32 v52, v52, v10, v28
	v_ashrrev_i32_e32 v53, 31, v52
	v_lshl_add_u64 v[52:53], v[52:53], 4, s[10:11]
	s_cbranch_execz .Lkb_p2_st0
	global_store_dwordx4 v[52:53], v[36:39], off

.LBB1_32:
	s_endpgm
	s_endpgm
